# layer-0 expert GEMM2: first K-tile of every unit peeled with C = 0 (accumulator-zeroing moves removed), on top of the best version
# baseline (speedup 1.0000x reference)
; #define LAS __attribute__((address_space(3)))
; template <class Epi, class Sched, bool GATHER, bool FP8 = false>
; __device__ __forceinline__ void gemm_phase(LAS unsigned char* lds, LAS int* idx, const Gemm g, const Sched& S, const Epi& E) {
;     ...
;         const char* nA = (has_next && !GATHER) ? (const char*)g.A + (size_t)nxt.pm * tstep + (size_t)nxt.be * g.astride : cA;
;         const char* nB = has_next ? (const char*)g.Bt + (size_t)nxt.be * g.bstride + (size_t)nxt.pn * tstep : cB;
;         if constexpr (GATHER) {
;             if (has_next && wid == 0) __builtin_amdgcn_global_load_lds((const unsigned*)(g.gather + (size_t)nxt.pm * BM + lane * 4), (LAS unsigned*)(idx + ((ui + 1) & 1) * BM), 16, 0, 0);
;         }
;         int t = 0;
;         do {
;             const bool last = (t == nt - 2);
;             const char* a1 = cA + (size_t)(t + 1) * kstep;
;             const char* a2 = last ? nA : cA + (size_t)(t + 2) * kstep; const char* b2 = last ? nB : cB + (size_t)(t + 2) * kstep;
;             const char* a3 = a2 + kstep; const char* b3 = b2 + kstep;
;             const size_t k1 = (size_t)(t + 1) * kstep, k2 = last ? (size_t)0 : (size_t)(t + 2) * kstep, k3 = k2 + kstep;
;     ...
; #pragma unroll
;         for (int a = 0; a < 2; ++a)
; #pragma unroll
;             for (int b = 0; b < 2; ++b)
; #pragma unroll
;                 for (int m = 0; m < 4; ++m)
; #pragma unroll
;                     for (int n = 0; n < 2; ++n) acc[a][b][m][n] = (f32x4){0.f, 0.f, 0.f, 0.f};
;         cur = nxt; cA = nA; cB = nB; ++ui;
.LBB0_856:
	s_cmp_lg_u32 s22, 0
	s_cselect_b64 s[22:23], -1, 0
	s_add_u32 s64, s24, 0x100
	s_mov_b32 s15, 0
	s_addc_u32 s65, s25, 0
	v_lshl_add_u64 v[206:207], s[20:21], 0, v[202:203]
	v_lshl_add_u64 v[208:209], s[20:21], 0, v[204:205]
	s_mov_b64 s[24:25], 0
	s_branch .Lpl858_858

; #define PG8_STAGE(bufoff, gbase, voff) do { _Pragma("unroll") for (int _i = 0; _i < 2; ++_i) \
;         __builtin_amdgcn_global_load_lds((const unsigned*)((const char*)(gbase) + (voff)[_i]), (LAS unsigned*)(lds + (bufoff) + ldsw + _i * 8192), 16, 0, 0); } while (0)
; #define PG8_STAGEA(bufoff, h, ap, kb, go) do { if constexpr (GATHER) { PG8_STAGE(bufoff, (const char*)g.A + (kb), go[h]); } else { PG8_STAGE(bufoff, (ap) + (h) * hstep, voffA); } } while (0)
; #define PG8_WAIT_V(n) asm volatile("s_waitcnt vmcnt(" #n ")" ::: "memory")
; #define PG8_WAIT_L(n) asm volatile("s_waitcnt lgkmcnt(" #n ")" ::: "memory")
; #define PG8_BAR __builtin_amdgcn_s_barrier()
; #define PG8_SCHED __builtin_amdgcn_sched_barrier(0)
; template <class Epi, class Sched, bool GATHER, bool FP8 = false>
; __device__ __forceinline__ void gemm_phase(LAS unsigned char* lds, LAS int* idx, const Gemm g, const Sched& S, const Epi& E) {
;     ...
;             PG8_LDB(B0, 1, 0); PG8_LDB(B1, 1, 1); PG8_SCHED; PG8_LDA(At, 1, 0); PG8_STAGEA(PG8_SA(0, 1), 1, a2, k2, g2);
;             PG8_WAIT_V(8); PG8_WAIT_L(0); PG8_BAR; PG8_MMA(0, 0, At, B0); PG8_MMA(0, 1, At, B1); PG8_BAR; PG8_SCHED;
;             PG8_LDA(At, 1, 1); PG8_STAGE(PG8_SB(1, 0), b3, voffB); PG8_STAGE(PG8_SB(1, 1), b3 + hstepB, voffB); PG8_STAGEA(PG8_SA(1, 0), 0, a3, k3, g2);
;             PG8_WAIT_V(8); PG8_WAIT_L(0); PG8_BAR; PG8_MMA(1, 0, At, B0); PG8_MMA(1, 1, At, B1); PG8_BAR; PG8_SCHED;
;             if constexpr (GATHER) { if (last) { _Pragma("unroll") for (int h = 0; h < 2; ++h) _Pragma("unroll") for (int i = 0; i < 2; ++i) gc[h][i] = g2[h][i]; } }
;             t += 2;
;         } while (t < nt);
.Lpl858_join:
	s_setprio 0
	s_barrier
	ds_read_b128 v[2:5], v232
	ds_read_b128 v[6:9], v233
	ds_read_b128 v[10:13], v234
	ds_read_b128 v[14:17], v235
	ds_read_b128 v[18:21], v236
	ds_read_b128 v[22:25], v237
	ds_read_b128 v[26:29], v238
	ds_read_b128 v[30:33], v239
	s_add_u32 s26, s26, s2
	s_addc_u32 s27, s27, s3
	s_mov_b32 m0, s47
	v_lshl_add_u64 v[246:247], s[26:27], 0, v[194:195]
	ds_read_b128 v[34:37], v241 offset:32768
	ds_read_b128 v[38:41], v241 offset:33792
	ds_read_b128 v[42:45], v241 offset:34816
	ds_read_b128 v[46:49], v241 offset:35840
	ds_read_b128 v[50:53], v241 offset:36864
	ds_read_b128 v[54:57], v241 offset:37888
	ds_read_b128 v[58:61], v241 offset:38912
	ds_read_b128 v[62:65], v241 offset:39936
	global_load_lds_dwordx4 v[246:247], off
	v_lshl_add_u64 v[246:247], s[26:27], 0, v[198:199]
	s_mov_b32 m0, s48
	s_nop 0
	global_load_lds_dwordx4 v[246:247], off
	s_waitcnt vmcnt(8)
	s_waitcnt lgkmcnt(0)
	s_barrier
	s_setprio 1
	s_waitcnt lgkmcnt(0)
	v_mfma_scale_f32_16x16x128_f8f6f4 v[190:193], v[2:9], v[34:41], v[190:193], v242, v243 op_sel_hi:[0,0,0]
	v_mfma_scale_f32_16x16x128_f8f6f4 v[186:189], v[10:17], v[34:41], v[186:189], v242, v243 op_sel_hi:[0,0,0]
	v_mfma_scale_f32_16x16x128_f8f6f4 v[178:181], v[2:9], v[42:49], v[178:181], v242, v243 op_sel_hi:[0,0,0]
	v_mfma_scale_f32_16x16x128_f8f6f4 v[170:173], v[10:17], v[42:49], v[170:173], v242, v243 op_sel_hi:[0,0,0]
	v_mfma_scale_f32_16x16x128_f8f6f4 v[162:165], v[2:9], v[50:57], v[162:165], v242, v243 op_sel_hi:[0,0,0]
	v_mfma_scale_f32_16x16x128_f8f6f4 v[154:157], v[10:17], v[50:57], v[154:157], v242, v243 op_sel_hi:[0,0,0]
	v_mfma_scale_f32_16x16x128_f8f6f4 v[146:149], v[2:9], v[58:65], v[146:149], v242, v243 op_sel_hi:[0,0,0]
	v_mfma_scale_f32_16x16x128_f8f6f4 v[138:141], v[10:17], v[58:65], v[138:141], v242, v243 op_sel_hi:[0,0,0]
	s_setprio 0
	s_setprio 1
	v_mfma_scale_f32_16x16x128_f8f6f4 v[182:185], v[18:25], v[34:41], v[182:185], v242, v243 op_sel_hi:[0,0,0]
	v_mfma_scale_f32_16x16x128_f8f6f4 v[174:177], v[26:33], v[34:41], v[174:177], v242, v243 op_sel_hi:[0,0,0]
	v_mfma_scale_f32_16x16x128_f8f6f4 v[166:169], v[18:25], v[42:49], v[166:169], v242, v243 op_sel_hi:[0,0,0]
	v_mfma_scale_f32_16x16x128_f8f6f4 v[158:161], v[26:33], v[42:49], v[158:161], v242, v243 op_sel_hi:[0,0,0]
	v_mfma_scale_f32_16x16x128_f8f6f4 v[150:153], v[18:25], v[50:57], v[150:153], v242, v243 op_sel_hi:[0,0,0]
	v_mfma_scale_f32_16x16x128_f8f6f4 v[142:145], v[26:33], v[50:57], v[142:145], v242, v243 op_sel_hi:[0,0,0]
	v_mfma_scale_f32_16x16x128_f8f6f4 v[134:137], v[18:25], v[58:65], v[134:137], v242, v243 op_sel_hi:[0,0,0]
	v_mfma_scale_f32_16x16x128_f8f6f4 v[130:133], v[26:33], v[58:65], v[130:133], v242, v243 op_sel_hi:[0,0,0]
	s_setprio 0
	s_barrier
	s_mov_b32 m0, s49
	v_lshl_add_u64 v[210:211], v[210:211], 0, s[10:11]
	ds_read_b128 v[34:37], v241 offset:49152
	ds_read_b128 v[38:41], v241 offset:50176
	ds_read_b128 v[42:45], v241 offset:51200
	ds_read_b128 v[46:49], v241 offset:52224
	ds_read_b128 v[50:53], v241 offset:53248
	ds_read_b128 v[54:57], v241 offset:54272
	ds_read_b128 v[58:61], v241 offset:55296
	ds_read_b128 v[62:65], v241 offset:56320
	global_load_lds_dwordx4 v[210:211], off
	v_lshl_add_u64 v[210:211], v[212:213], 0, s[10:11]
	s_mov_b32 m0, s50
	s_nop 0
	global_load_lds_dwordx4 v[210:211], off
	v_lshl_add_u64 v[210:211], v[214:215], 0, s[10:11]
	s_mov_b32 m0, s53
	s_nop 0
	global_load_lds_dwordx4 v[210:211], off
	v_lshl_add_u64 v[210:211], v[216:217], 0, s[10:11]
	s_mov_b32 m0, s54
	s_nop 0
	global_load_lds_dwordx4 v[210:211], off
	v_lshl_add_u64 v[210:211], v[218:219], 0, s[10:11]
	s_mov_b32 m0, s51
	s_nop 0
	global_load_lds_dwordx4 v[210:211], off
	v_lshl_add_u64 v[210:211], v[220:221], 0, s[10:11]
	s_mov_b32 m0, s52
	s_nop 0
	global_load_lds_dwordx4 v[210:211], off
	s_waitcnt vmcnt(8)
	s_waitcnt lgkmcnt(0)
	s_barrier
	s_setprio 1
	s_waitcnt lgkmcnt(0)
	v_mfma_scale_f32_16x16x128_f8f6f4 v[126:129], v[2:9], v[34:41], v[126:129], v242, v243 op_sel_hi:[0,0,0]
	v_mfma_scale_f32_16x16x128_f8f6f4 v[122:125], v[10:17], v[34:41], v[122:125], v242, v243 op_sel_hi:[0,0,0]
	v_mfma_scale_f32_16x16x128_f8f6f4 v[114:117], v[2:9], v[42:49], v[114:117], v242, v243 op_sel_hi:[0,0,0]
	v_mfma_scale_f32_16x16x128_f8f6f4 v[106:109], v[10:17], v[42:49], v[106:109], v242, v243 op_sel_hi:[0,0,0]
	v_mfma_scale_f32_16x16x128_f8f6f4 v[98:101], v[2:9], v[50:57], v[98:101], v242, v243 op_sel_hi:[0,0,0]
	v_mfma_scale_f32_16x16x128_f8f6f4 v[90:93], v[10:17], v[50:57], v[90:93], v242, v243 op_sel_hi:[0,0,0]
	v_mfma_scale_f32_16x16x128_f8f6f4 v[82:85], v[2:9], v[58:65], v[82:85], v242, v243 op_sel_hi:[0,0,0]
	v_mfma_scale_f32_16x16x128_f8f6f4 v[74:77], v[10:17], v[58:65], v[74:77], v242, v243 op_sel_hi:[0,0,0]
	s_setprio 0
	s_setprio 1
	v_mfma_scale_f32_16x16x128_f8f6f4 v[118:121], v[18:25], v[34:41], v[118:121], v242, v243 op_sel_hi:[0,0,0]
	v_mfma_scale_f32_16x16x128_f8f6f4 v[110:113], v[26:33], v[34:41], v[110:113], v242, v243 op_sel_hi:[0,0,0]
	v_mfma_scale_f32_16x16x128_f8f6f4 v[102:105], v[18:25], v[42:49], v[102:105], v242, v243 op_sel_hi:[0,0,0]
	v_mfma_scale_f32_16x16x128_f8f6f4 v[94:97], v[26:33], v[42:49], v[94:97], v242, v243 op_sel_hi:[0,0,0]
	v_mfma_scale_f32_16x16x128_f8f6f4 v[86:89], v[18:25], v[50:57], v[86:89], v242, v243 op_sel_hi:[0,0,0]
	v_mfma_scale_f32_16x16x128_f8f6f4 v[78:81], v[26:33], v[50:57], v[78:81], v242, v243 op_sel_hi:[0,0,0]
	v_mfma_scale_f32_16x16x128_f8f6f4 v[70:73], v[18:25], v[58:65], v[70:73], v242, v243 op_sel_hi:[0,0,0]
	v_mfma_scale_f32_16x16x128_f8f6f4 v[66:69], v[26:33], v[58:65], v[66:69], v242, v243 op_sel_hi:[0,0,0]
	s_setprio 0
	s_barrier
	s_add_u32 s24, s24, 0x100
	s_addc_u32 s25, s25, 0
	s_cmp_lt_i32 s15, s56
	s_cbranch_scc0 .LBB0_866

; #define PG8_STAGEA(bufoff, h, ap, kb, go) do { if constexpr (GATHER) { PG8_STAGE(bufoff, (const char*)g.A + (kb), go[h]); } else { PG8_STAGE(bufoff, (ap) + (h) * hstep, voffA); } } while (0)
; #define PG8_WAIT_L(n) asm volatile("s_waitcnt lgkmcnt(" #n ")" ::: "memory")
; #define PG8_WAIT_V8R() do { if (relax) { if (GATHER && wid == 0 && has_next) asm volatile("s_waitcnt vmcnt(%0)" :: "n"(9 + Epi::NSTORES) : "memory"); else asm volatile("s_waitcnt vmcnt(%0)" :: "n"(8 + Epi::NSTORES) : "memory"); } else PG8_WAIT_V(8); } while (0)
; #define PG8_BAR __builtin_amdgcn_s_barrier()
; #define PG8_SCHED __builtin_amdgcn_sched_barrier(0)
; #define PG8_GIDX(dst, base) do { _Pragma("unroll") for (int i = 0; i < 2; ++i) { int R_, C_; stage_rc(tid * 16 + i * 8192, R_, C_); _Pragma("unroll") for (int h = 0; h < 2; ++h) dst[h][i] = (unsigned)idx[(base) + h * HALF + R_] * rowB + (unsigned)C_ * 2u; } } while (0)
; template <class Epi, class Sched, bool GATHER, bool FP8 = false>
; __device__ __forceinline__ void gemm_phase(LAS unsigned char* lds, LAS int* idx, const Gemm g, const Sched& S, const Epi& E) {
;     ...
;             const char* a2 = last ? nA : cA + (size_t)(t + 2) * kstep; const char* b2 = last ? nB : cB + (size_t)(t + 2) * kstep;
;             const char* a3 = a2 + kstep; const char* b3 = b2 + kstep;
;             const size_t k1 = (size_t)(t + 1) * kstep, k2 = last ? (size_t)0 : (size_t)(t + 2) * kstep, k3 = k2 + kstep;
;             unsigned g2[2][2];
; #pragma unroll
;             for (int h = 0; h < 2; ++h)
; #pragma unroll
;                 for (int i = 0; i < 2; ++i) g2[h][i] = gc[h][i];
;             if constexpr (GATHER) { if (last && has_next) PG8_GIDX(g2, ((ui + 1) & 1) * BM); }
;             const int relax = __builtin_amdgcn_readfirstlane(((t == 0) && (ui > 0)) ? 1 : 0);
;             PG8_LDB(B0, 0, 0); PG8_LDB(B1, 0, 1); PG8_SCHED; PG8_LDA(At, 0, 0); PG8_STAGEA(PG8_SA(1, 1), 1, a1, k1, gc);
;             PG8_WAIT_V8R(); PG8_WAIT_L(0); PG8_BAR; PG8_MMA(0, 0, At, B0); PG8_MMA(0, 1, At, B1); PG8_BAR; PG8_SCHED;
.LBB0_864:
	s_andn2_b64 vcc, exec, s[30:31]
	s_cbranch_vccnz .LBB0_857
	s_waitcnt vmcnt(16)
	s_branch .LBB0_857
.Lpl858_858:
	ds_read_b128 v[26:29], v222
	ds_read_b128 v[30:33], v223
	ds_read_b128 v[18:21], v224
	ds_read_b128 v[22:25], v225
	ds_read_b128 v[10:13], v226
	ds_read_b128 v[14:17], v227
	ds_read_b128 v[2:5], v228
	ds_read_b128 v[6:9], v229
	s_cmp_eq_u32 s15, 0
	s_cselect_b64 s[26:27], -1, 0
	s_and_b64 s[26:27], s[22:23], s[26:27]
	v_lshl_add_u64 v[210:211], v[206:207], 0, s[24:25]
	s_add_i32 m0, s41, 0xc000
	ds_read_b128 v[58:61], v241
	ds_read_b128 v[62:65], v241 offset:1024
	ds_read_b128 v[50:53], v241 offset:2048
	ds_read_b128 v[54:57], v241 offset:3072
	ds_read_b128 v[42:45], v241 offset:4096
	ds_read_b128 v[46:49], v241 offset:5120
	ds_read_b128 v[34:37], v241 offset:6144
	ds_read_b128 v[38:41], v241 offset:7168
	global_load_lds_dwordx4 v[210:211], off
	v_lshl_add_u64 v[210:211], v[208:209], 0, s[24:25]
	s_add_i32 m0, s41, 0xe000
	s_nop 0
	global_load_lds_dwordx4 v[210:211], off
	s_and_b64 vcc, exec, s[26:27]
	s_not_b64 s[28:29], s[26:27]
	s_mov_b64 s[26:27], -1
	s_cbranch_vccnz .Lpl858_860
	s_waitcnt vmcnt(8)
	s_mov_b64 s[26:27], 0

; #define PG8_STAGE(bufoff, gbase, voff) do { _Pragma("unroll") for (int _i = 0; _i < 2; ++_i) \
;         __builtin_amdgcn_global_load_lds((const unsigned*)((const char*)(gbase) + (voff)[_i]), (LAS unsigned*)(lds + (bufoff) + ldsw + _i * 8192), 16, 0, 0); } while (0)
; #define PG8_STAGEA(bufoff, h, ap, kb, go) do { if constexpr (GATHER) { PG8_STAGE(bufoff, (const char*)g.A + (kb), go[h]); } else { PG8_STAGE(bufoff, (ap) + (h) * hstep, voffA); } } while (0)
; #define PG8_WAIT_L(n) asm volatile("s_waitcnt lgkmcnt(" #n ")" ::: "memory")
; #define PG8_WAIT_V8R() do { if (relax) { if (GATHER && wid == 0 && has_next) asm volatile("s_waitcnt vmcnt(%0)" :: "n"(9 + Epi::NSTORES) : "memory"); else asm volatile("s_waitcnt vmcnt(%0)" :: "n"(8 + Epi::NSTORES) : "memory"); } else PG8_WAIT_V(8); } while (0)
; #define PG8_BAR __builtin_amdgcn_s_barrier()
; #define PG8_SCHED __builtin_amdgcn_sched_barrier(0)
; template <class Epi, class Sched, bool GATHER, bool FP8 = false>
; __device__ __forceinline__ void gemm_phase(LAS unsigned char* lds, LAS int* idx, const Gemm g, const Sched& S, const Epi& E) {
;     ...
;             PG8_WAIT_V8R(); PG8_WAIT_L(0); PG8_BAR; PG8_MMA(0, 0, At, B0); PG8_MMA(0, 1, At, B1); PG8_BAR; PG8_SCHED;
;             PG8_LDA(At, 0, 1); PG8_STAGE(PG8_SB(0, 0), b2, voffB); PG8_STAGE(PG8_SB(0, 1), b2 + hstepB, voffB); PG8_STAGEA(PG8_SA(0, 0), 0, a2, k2, g2);
;             PG8_WAIT_V8R(); PG8_WAIT_L(0); PG8_BAR; PG8_MMA(1, 0, At, B0); PG8_MMA(1, 1, At, B1); PG8_BAR; PG8_SCHED;
.Lpl858_862:
	s_add_u32 s26, s20, s24
	s_addc_u32 s27, s21, s25
	s_add_u32 s26, s26, 0x100
	s_addc_u32 s27, s27, 0
	s_add_u32 s30, s64, s24
	s_addc_u32 s31, s65, s25
	s_waitcnt lgkmcnt(0)
	s_cmp_eq_u32 s57, s15
	s_cselect_b32 s27, s17, s27
	s_cselect_b32 s26, s16, s26
	s_cselect_b32 s31, s19, s31
	s_cselect_b32 s30, s18, s30
	s_barrier
	s_setprio 1
	s_waitcnt lgkmcnt(0)
	v_mfma_scale_f32_16x16x128_f8f6f4 v[190:193], v[26:33], v[58:65], 0, v242, v243 op_sel_hi:[0,0,0]
	v_mfma_scale_f32_16x16x128_f8f6f4 v[186:189], v[18:25], v[58:65], 0, v242, v243 op_sel_hi:[0,0,0]
	v_mfma_scale_f32_16x16x128_f8f6f4 v[178:181], v[26:33], v[50:57], 0, v242, v243 op_sel_hi:[0,0,0]
	v_mfma_scale_f32_16x16x128_f8f6f4 v[170:173], v[18:25], v[50:57], 0, v242, v243 op_sel_hi:[0,0,0]
	v_mfma_scale_f32_16x16x128_f8f6f4 v[162:165], v[26:33], v[42:49], 0, v242, v243 op_sel_hi:[0,0,0]
	v_mfma_scale_f32_16x16x128_f8f6f4 v[154:157], v[18:25], v[42:49], 0, v242, v243 op_sel_hi:[0,0,0]
	v_mfma_scale_f32_16x16x128_f8f6f4 v[146:149], v[26:33], v[34:41], 0, v242, v243 op_sel_hi:[0,0,0]
	v_mfma_scale_f32_16x16x128_f8f6f4 v[138:141], v[18:25], v[34:41], 0, v242, v243 op_sel_hi:[0,0,0]
	s_setprio 0
	s_setprio 1
	v_mfma_scale_f32_16x16x128_f8f6f4 v[182:185], v[10:17], v[58:65], 0, v242, v243 op_sel_hi:[0,0,0]
	v_mfma_scale_f32_16x16x128_f8f6f4 v[174:177], v[2:9], v[58:65], 0, v242, v243 op_sel_hi:[0,0,0]
	v_mfma_scale_f32_16x16x128_f8f6f4 v[166:169], v[10:17], v[50:57], 0, v242, v243 op_sel_hi:[0,0,0]
	v_mfma_scale_f32_16x16x128_f8f6f4 v[158:161], v[2:9], v[50:57], 0, v242, v243 op_sel_hi:[0,0,0]
	v_mfma_scale_f32_16x16x128_f8f6f4 v[150:153], v[10:17], v[42:49], 0, v242, v243 op_sel_hi:[0,0,0]
	v_mfma_scale_f32_16x16x128_f8f6f4 v[142:145], v[2:9], v[42:49], 0, v242, v243 op_sel_hi:[0,0,0]
	v_mfma_scale_f32_16x16x128_f8f6f4 v[134:137], v[10:17], v[34:41], 0, v242, v243 op_sel_hi:[0,0,0]
	v_mfma_scale_f32_16x16x128_f8f6f4 v[130:133], v[2:9], v[34:41], 0, v242, v243 op_sel_hi:[0,0,0]
	s_setprio 0
	s_barrier
	s_mov_b32 m0, s42
	v_lshl_add_u64 v[210:211], s[30:31], 0, v[196:197]
	v_lshl_add_u64 v[212:213], s[30:31], 0, v[200:201]
	s_add_u32 s30, s30, s6
	ds_read_b128 v[58:61], v241 offset:16384
	ds_read_b128 v[62:65], v241 offset:17408
	ds_read_b128 v[50:53], v241 offset:18432
	ds_read_b128 v[54:57], v241 offset:19456
	ds_read_b128 v[42:45], v241 offset:20480
	ds_read_b128 v[46:49], v241 offset:21504
	ds_read_b128 v[34:37], v241 offset:22528
	ds_read_b128 v[38:41], v241 offset:23552
	global_load_lds_dwordx4 v[210:211], off
	s_mov_b32 m0, s43
	s_addc_u32 s31, s31, s7
	global_load_lds_dwordx4 v[212:213], off
	v_lshl_add_u64 v[214:215], s[30:31], 0, v[196:197]
	s_mov_b32 m0, s44
	v_lshl_add_u64 v[216:217], s[30:31], 0, v[200:201]
	global_load_lds_dwordx4 v[214:215], off
	s_mov_b32 m0, s45
	v_lshl_add_u64 v[218:219], s[26:27], 0, v[194:195]
	global_load_lds_dwordx4 v[216:217], off
	s_mov_b32 m0, s41
	v_lshl_add_u64 v[220:221], s[26:27], 0, v[198:199]
	global_load_lds_dwordx4 v[218:219], off
	s_mov_b32 m0, s46
	s_mov_b64 s[30:31], -1
	global_load_lds_dwordx4 v[220:221], off
	s_and_b64 vcc, exec, s[28:29]
	s_cbranch_vccz .Lpl858_864
	s_waitcnt vmcnt(8)
	s_mov_b64 s[30:31], 0

; #define PG8_STAGE(bufoff, gbase, voff) do { _Pragma("unroll") for (int _i = 0; _i < 2; ++_i) \
;         __builtin_amdgcn_global_load_lds((const unsigned*)((const char*)(gbase) + (voff)[_i]), (LAS unsigned*)(lds + (bufoff) + ldsw + _i * 8192), 16, 0, 0); } while (0)
; #define PG8_STAGEA(bufoff, h, ap, kb, go) do { if constexpr (GATHER) { PG8_STAGE(bufoff, (const char*)g.A + (kb), go[h]); } else { PG8_STAGE(bufoff, (ap) + (h) * hstep, voffA); } } while (0)
; #define PG8_WAIT_V(n) asm volatile("s_waitcnt vmcnt(" #n ")" ::: "memory")
; #define PG8_WAIT_L(n) asm volatile("s_waitcnt lgkmcnt(" #n ")" ::: "memory")
; #define PG8_WAIT_V8R() do { if (relax) { if (GATHER && wid == 0 && has_next) asm volatile("s_waitcnt vmcnt(%0)" :: "n"(9 + Epi::NSTORES) : "memory"); else asm volatile("s_waitcnt vmcnt(%0)" :: "n"(8 + Epi::NSTORES) : "memory"); } else PG8_WAIT_V(8); } while (0)
; #define PG8_BAR __builtin_amdgcn_s_barrier()
; #define PG8_SCHED __builtin_amdgcn_sched_barrier(0)
; template <class Epi, class Sched, bool GATHER, bool FP8 = false>
; __device__ __forceinline__ void gemm_phase(LAS unsigned char* lds, LAS int* idx, const Gemm g, const Sched& S, const Epi& E) {
;     ...
;             PG8_WAIT_V8R(); PG8_WAIT_L(0); PG8_BAR; PG8_MMA(1, 0, At, B0); PG8_MMA(1, 1, At, B1); PG8_BAR; PG8_SCHED;
;             PG8_LDB(B0, 1, 0); PG8_LDB(B1, 1, 1); PG8_SCHED; PG8_LDA(At, 1, 0); PG8_STAGEA(PG8_SA(0, 1), 1, a2, k2, g2);
;             PG8_WAIT_V(8); PG8_WAIT_L(0); PG8_BAR; PG8_MMA(0, 0, At, B0); PG8_MMA(0, 1, At, B1); PG8_BAR; PG8_SCHED;
;             PG8_LDA(At, 1, 1); PG8_STAGE(PG8_SB(1, 0), b3, voffB); PG8_STAGE(PG8_SB(1, 1), b3 + hstepB, voffB); PG8_STAGEA(PG8_SA(1, 0), 0, a3, k3, g2);
;             PG8_WAIT_V(8); PG8_WAIT_L(0); PG8_BAR; PG8_MMA(1, 0, At, B0); PG8_MMA(1, 1, At, B1); PG8_BAR; PG8_SCHED;
;             if constexpr (GATHER) { if (last) { _Pragma("unroll") for (int h = 0; h < 2; ++h) _Pragma("unroll") for (int i = 0; i < 2; ++i) gc[h][i] = g2[h][i]; } }
;             t += 2;
.Lpl858_857:
	s_waitcnt lgkmcnt(0)
	s_add_i32 s15, s15, 2
	s_barrier
	s_setprio 1
	s_waitcnt lgkmcnt(0)
	v_mfma_scale_f32_16x16x128_f8f6f4 v[126:129], v[26:33], v[58:65], 0, v242, v243 op_sel_hi:[0,0,0]
	v_mfma_scale_f32_16x16x128_f8f6f4 v[122:125], v[18:25], v[58:65], 0, v242, v243 op_sel_hi:[0,0,0]
	v_mfma_scale_f32_16x16x128_f8f6f4 v[114:117], v[26:33], v[50:57], 0, v242, v243 op_sel_hi:[0,0,0]
	v_mfma_scale_f32_16x16x128_f8f6f4 v[106:109], v[18:25], v[50:57], 0, v242, v243 op_sel_hi:[0,0,0]
	v_mfma_scale_f32_16x16x128_f8f6f4 v[98:101], v[26:33], v[42:49], 0, v242, v243 op_sel_hi:[0,0,0]
	v_mfma_scale_f32_16x16x128_f8f6f4 v[90:93], v[18:25], v[42:49], 0, v242, v243 op_sel_hi:[0,0,0]
	v_mfma_scale_f32_16x16x128_f8f6f4 v[82:85], v[26:33], v[34:41], 0, v242, v243 op_sel_hi:[0,0,0]
	v_mfma_scale_f32_16x16x128_f8f6f4 v[74:77], v[18:25], v[34:41], 0, v242, v243 op_sel_hi:[0,0,0]
	s_setprio 0
	s_setprio 1
	v_mfma_scale_f32_16x16x128_f8f6f4 v[118:121], v[10:17], v[58:65], 0, v242, v243 op_sel_hi:[0,0,0]
	v_mfma_scale_f32_16x16x128_f8f6f4 v[110:113], v[2:9], v[58:65], 0, v242, v243 op_sel_hi:[0,0,0]
	v_mfma_scale_f32_16x16x128_f8f6f4 v[102:105], v[10:17], v[50:57], 0, v242, v243 op_sel_hi:[0,0,0]
	v_mfma_scale_f32_16x16x128_f8f6f4 v[94:97], v[2:9], v[50:57], 0, v242, v243 op_sel_hi:[0,0,0]
	v_mfma_scale_f32_16x16x128_f8f6f4 v[86:89], v[10:17], v[42:49], 0, v242, v243 op_sel_hi:[0,0,0]
	v_mfma_scale_f32_16x16x128_f8f6f4 v[78:81], v[2:9], v[42:49], 0, v242, v243 op_sel_hi:[0,0,0]
	v_mfma_scale_f32_16x16x128_f8f6f4 v[70:73], v[10:17], v[34:41], 0, v242, v243 op_sel_hi:[0,0,0]
	v_mfma_scale_f32_16x16x128_f8f6f4 v[66:69], v[2:9], v[34:41], 0, v242, v243 op_sel_hi:[0,0,0]
	s_branch .Lpl858_join
